# baseline (speedup 1.0000x reference)
.LBB1_4:
	s_load_dwordx2 s[0:1], s[0:1], 0x0
	v_add_u32_e32 v2, 0xffffff00, v0
	v_ashrrev_i32_e32 v20, 4, v2
	v_add_u32_e32 v2, s12, v20
	v_ashrrev_i32_e32 v3, 31, v2
	v_lshlrev_b64 v[2:3], 12, v[2:3]
	s_lshl_b32 s2, s3, 6
	s_waitcnt lgkmcnt(0)
	v_lshl_add_u64 v[2:3], s[0:1], 0, v[2:3]
	v_lshlrev_b32_e32 v4, 4, v1
	v_mov_b32_e32 v5, 0
	s_and_b32 s6, s2, 0x3c0
	s_mov_b32 s1, 0
	v_lshl_add_u64 v[2:3], v[2:3], 0, v[4:5]
	s_lshl_b32 s0, s6, 2
	v_lshl_add_u64 v[16:17], v[2:3], 0, s[0:1]
	s_mov_b32 s3, 0x10000
	v_add_co_u32_e32 v12, vcc, s3, v16
	s_mov_b32 s4, 0x20000
	s_nop 0
	v_addc_co_u32_e32 v13, vcc, 0, v17, vcc
	global_load_dwordx4 v[4:7], v[16:17], off sc1 nt
	global_load_dwordx4 v[8:11], v[12:13], off sc1 nt
	v_add_co_u32_e32 v12, vcc, s4, v16
	s_mov_b32 s5, 0x30000
	s_nop 0
	v_addc_co_u32_e32 v13, vcc, 0, v17, vcc
	s_add_i32 s0, s2, 64
	global_load_dwordx4 v[12:15], v[12:13], off sc1 nt
	v_add_co_u32_e32 v16, vcc, s5, v16
	s_and_b32 s0, s0, 0x3c0
	s_nop 0
	v_addc_co_u32_e32 v17, vcc, 0, v17, vcc
	s_lshl_b32 s0, s0, 2
	global_load_dwordx4 v[16:19], v[16:17], off sc1 nt
	v_lshl_add_u64 v[28:29], v[2:3], 0, s[0:1]
	v_lshrrev_b32_e32 v1, 1, v1
	v_lshrrev_b32_e32 v21, 5, v0
	v_lshlrev_b32_e32 v0, 3, v0
	v_add_co_u32_e32 v30, vcc, s3, v28
	v_bitop3_b32 v1, v1, v21, 7 bitop3:0x78
	v_and_b32_e32 v0, 8, v0
	v_addc_co_u32_e32 v31, vcc, 0, v29, vcc
	v_lshl_or_b32 v0, v1, 4, v0
	v_add_co_u32_e32 v36, vcc, s4, v28
	v_lshl_or_b32 v0, v20, 7, v0
	global_load_dwordx4 v[20:23], v[28:29], off sc1 nt
	global_load_dwordx4 v[24:27], v[30:31], off sc1 nt
	v_addc_co_u32_e32 v37, vcc, 0, v29, vcc
	s_add_i32 s0, s2, 0x80
	v_add_co_u32_e32 v38, vcc, s5, v28
	s_and_b32 s0, s0, 0x3c0
	s_nop 0
	v_addc_co_u32_e32 v39, vcc, 0, v29, vcc
	global_load_dwordx4 v[28:31], v[36:37], off sc1 nt
	global_load_dwordx4 v[32:35], v[38:39], off sc1 nt
	s_lshl_b32 s0, s0, 2
	v_lshl_add_u64 v[44:45], v[2:3], 0, s[0:1]
	v_add_co_u32_e32 v46, vcc, s3, v44
	s_add_i32 s0, s2, 0xc0
	s_nop 0
	v_addc_co_u32_e32 v47, vcc, 0, v45, vcc
	v_add_co_u32_e32 v52, vcc, s4, v44
	global_load_dwordx4 v[36:39], v[44:45], off sc1 nt
	global_load_dwordx4 v[40:43], v[46:47], off sc1 nt
	v_addc_co_u32_e32 v53, vcc, 0, v45, vcc
	v_add_co_u32_e32 v54, vcc, s5, v44
	s_and_b32 s0, s0, 0x3c0
	s_nop 0
	v_addc_co_u32_e32 v55, vcc, 0, v45, vcc
	global_load_dwordx4 v[44:47], v[52:53], off sc1 nt
	global_load_dwordx4 v[48:51], v[54:55], off sc1 nt
	s_lshl_b32 s0, s0, 2
	v_lshl_add_u64 v[60:61], v[2:3], 0, s[0:1]
	v_add_co_u32_e32 v62, vcc, s3, v60
	s_add_i32 s0, s2, 0x100
	s_nop 0
	v_addc_co_u32_e32 v63, vcc, 0, v61, vcc
	v_add_co_u32_e32 v68, vcc, s4, v60
	global_load_dwordx4 v[52:55], v[60:61], off sc1 nt
	global_load_dwordx4 v[56:59], v[62:63], off sc1 nt
	v_addc_co_u32_e32 v69, vcc, 0, v61, vcc
	v_add_co_u32_e32 v70, vcc, s5, v60
	s_and_b32 s0, s0, 0x3c0
	s_nop 0
	v_addc_co_u32_e32 v71, vcc, 0, v61, vcc
	global_load_dwordx4 v[60:63], v[68:69], off sc1 nt
	global_load_dwordx4 v[64:67], v[70:71], off sc1 nt
	s_lshl_b32 s0, s0, 2
	v_add_u32_e32 v1, 0x10000, v0
	s_waitcnt vmcnt(15)
	v_cvt_pk_f16_f32 v7, v6, v7
	v_cvt_pk_f16_f32 v6, v4, v5
	s_waitcnt vmcnt(14)
	v_cvt_pk_f16_f32 v5, v10, v11
	v_cvt_pk_f16_f32 v4, v8, v9
	ds_write2st64_b64 v0, v[6:7], v[4:5] offset1:4
	s_waitcnt vmcnt(13)
	v_cvt_pk_f16_f32 v4, v12, v13
	v_lshl_add_u64 v[12:13], v[2:3], 0, s[0:1]
	v_cvt_pk_f16_f32 v5, v14, v15
	v_add_co_u32_e32 v14, vcc, s3, v12
	s_add_i32 s0, s2, 0x140
	s_nop 0
	v_addc_co_u32_e32 v15, vcc, 0, v13, vcc
	s_waitcnt vmcnt(12)
	v_cvt_pk_f16_f32 v7, v18, v19
	v_cvt_pk_f16_f32 v6, v16, v17
	ds_write2st64_b64 v0, v[4:5], v[6:7] offset0:8 offset1:12
	v_add_co_u32_e32 v68, vcc, s4, v12
	global_load_dwordx4 v[4:7], v[12:13], off sc1 nt
	global_load_dwordx4 v[8:11], v[14:15], off sc1 nt
	v_addc_co_u32_e32 v69, vcc, 0, v13, vcc
	v_add_co_u32_e32 v70, vcc, s5, v12
	s_and_b32 s0, s0, 0x3c0
	s_nop 0
	v_addc_co_u32_e32 v71, vcc, 0, v13, vcc
	global_load_dwordx4 v[12:15], v[68:69], off sc1 nt
	global_load_dwordx4 v[16:19], v[70:71], off sc1 nt
	s_waitcnt vmcnt(15)
	v_cvt_pk_f16_f32 v23, v22, v23
	v_cvt_pk_f16_f32 v22, v20, v21
	s_waitcnt vmcnt(14)
	v_cvt_pk_f16_f32 v21, v26, v27
	v_cvt_pk_f16_f32 v20, v24, v25
	s_lshl_b32 s0, s0, 2
	s_waitcnt lgkmcnt(0)
	s_barrier
	ds_write2st64_b64 v0, v[22:23], v[20:21] offset0:16 offset1:20
	s_waitcnt vmcnt(13)
	v_cvt_pk_f16_f32 v20, v28, v29
	v_lshl_add_u64 v[28:29], v[2:3], 0, s[0:1]
	v_cvt_pk_f16_f32 v21, v30, v31
	v_add_co_u32_e32 v30, vcc, s3, v28
	s_waitcnt vmcnt(12)
	v_cvt_pk_f16_f32 v23, v34, v35
	v_cvt_pk_f16_f32 v22, v32, v33
	v_addc_co_u32_e32 v31, vcc, 0, v29, vcc
	ds_write2st64_b64 v0, v[20:21], v[22:23] offset0:24 offset1:28
	v_add_co_u32_e32 v68, vcc, s4, v28
	global_load_dwordx4 v[20:23], v[28:29], off sc1 nt
	global_load_dwordx4 v[24:27], v[30:31], off sc1 nt
	v_addc_co_u32_e32 v69, vcc, 0, v29, vcc
	s_add_i32 s0, s2, 0x180
	v_add_co_u32_e32 v70, vcc, s5, v28
	s_and_b32 s0, s0, 0x3c0
	s_nop 0
	v_addc_co_u32_e32 v71, vcc, 0, v29, vcc
	global_load_dwordx4 v[28:31], v[68:69], off sc1 nt
	global_load_dwordx4 v[32:35], v[70:71], off sc1 nt
	s_waitcnt vmcnt(15)
	v_cvt_pk_f16_f32 v39, v38, v39
	v_cvt_pk_f16_f32 v38, v36, v37
	s_waitcnt vmcnt(14)
	v_cvt_pk_f16_f32 v37, v42, v43
	v_cvt_pk_f16_f32 v36, v40, v41
	s_lshl_b32 s0, s0, 2
	s_waitcnt lgkmcnt(0)
	s_barrier
	ds_write2st64_b64 v0, v[38:39], v[36:37] offset0:32 offset1:36
	s_waitcnt vmcnt(13)
	v_cvt_pk_f16_f32 v36, v44, v45
	v_lshl_add_u64 v[44:45], v[2:3], 0, s[0:1]
	v_cvt_pk_f16_f32 v37, v46, v47
	v_add_co_u32_e32 v46, vcc, s3, v44
	s_waitcnt vmcnt(12)
	v_cvt_pk_f16_f32 v39, v50, v51
	v_cvt_pk_f16_f32 v38, v48, v49
	v_addc_co_u32_e32 v47, vcc, 0, v45, vcc
	ds_write2st64_b64 v0, v[36:37], v[38:39] offset0:40 offset1:44
	v_add_co_u32_e32 v68, vcc, s4, v44
	global_load_dwordx4 v[36:39], v[44:45], off sc1 nt
	global_load_dwordx4 v[40:43], v[46:47], off sc1 nt
	v_addc_co_u32_e32 v69, vcc, 0, v45, vcc
	v_add_co_u32_e32 v70, vcc, s5, v44
	s_add_i32 s0, s2, 0x1c0
	s_nop 0
	v_addc_co_u32_e32 v71, vcc, 0, v45, vcc
	global_load_dwordx4 v[44:47], v[68:69], off sc1 nt
	global_load_dwordx4 v[48:51], v[70:71], off sc1 nt
	s_and_b32 s0, s0, 0x3c0
	s_waitcnt vmcnt(15)
	v_cvt_pk_f16_f32 v55, v54, v55
	v_cvt_pk_f16_f32 v54, v52, v53
	s_waitcnt vmcnt(14)
	v_cvt_pk_f16_f32 v53, v58, v59
	v_cvt_pk_f16_f32 v52, v56, v57
	s_lshl_b32 s0, s0, 2
	s_waitcnt lgkmcnt(0)
	s_barrier
	ds_write2st64_b64 v0, v[54:55], v[52:53] offset0:48 offset1:52
	s_waitcnt vmcnt(13)
	v_cvt_pk_f16_f32 v52, v60, v61
	v_lshl_add_u64 v[60:61], v[2:3], 0, s[0:1]
	v_cvt_pk_f16_f32 v53, v62, v63
	v_add_co_u32_e32 v62, vcc, s3, v60
	s_waitcnt vmcnt(12)
	v_cvt_pk_f16_f32 v55, v66, v67
	v_addc_co_u32_e32 v63, vcc, 0, v61, vcc
	v_cvt_pk_f16_f32 v54, v64, v65
	v_add_co_u32_e32 v68, vcc, s4, v60
	ds_write2st64_b64 v0, v[52:53], v[54:55] offset0:56 offset1:60
	s_nop 0
	v_addc_co_u32_e32 v69, vcc, 0, v61, vcc
	global_load_dwordx4 v[52:55], v[60:61], off sc1 nt
	global_load_dwordx4 v[56:59], v[62:63], off sc1 nt
	v_add_co_u32_e32 v70, vcc, s5, v60
	s_xor_b32 s0, s6, 0x200
	s_nop 0
	v_addc_co_u32_e32 v71, vcc, 0, v61, vcc
	global_load_dwordx4 v[60:63], v[68:69], off sc1 nt
	global_load_dwordx4 v[64:67], v[70:71], off sc1 nt
	s_waitcnt vmcnt(15)
	v_cvt_pk_f16_f32 v7, v6, v7
	v_cvt_pk_f16_f32 v6, v4, v5
	s_waitcnt vmcnt(14)
	v_cvt_pk_f16_f32 v5, v10, v11
	v_cvt_pk_f16_f32 v4, v8, v9
	s_lshl_b32 s0, s0, 2
	s_waitcnt lgkmcnt(0)
	s_barrier
	ds_write2st64_b64 v0, v[6:7], v[4:5] offset0:64 offset1:68
	s_waitcnt vmcnt(13)
	v_cvt_pk_f16_f32 v4, v12, v13
	v_lshl_add_u64 v[12:13], v[2:3], 0, s[0:1]
	v_cvt_pk_f16_f32 v5, v14, v15
	v_add_co_u32_e32 v14, vcc, s3, v12
	s_waitcnt vmcnt(12)
	v_cvt_pk_f16_f32 v7, v18, v19
	v_cvt_pk_f16_f32 v6, v16, v17
	v_addc_co_u32_e32 v15, vcc, 0, v13, vcc
	ds_write2st64_b64 v0, v[4:5], v[6:7] offset0:72 offset1:76
	v_add_co_u32_e32 v68, vcc, s4, v12
	global_load_dwordx4 v[4:7], v[12:13], off sc1 nt
	global_load_dwordx4 v[8:11], v[14:15], off sc1 nt
	v_addc_co_u32_e32 v69, vcc, 0, v13, vcc
	s_add_i32 s0, s2, 0x240
	v_add_co_u32_e32 v70, vcc, s5, v12
	s_and_b32 s0, s0, 0x3c0
	s_nop 0
	v_addc_co_u32_e32 v71, vcc, 0, v13, vcc
	global_load_dwordx4 v[12:15], v[68:69], off sc1 nt
	global_load_dwordx4 v[16:19], v[70:71], off sc1 nt
	s_waitcnt vmcnt(15)
	v_cvt_pk_f16_f32 v23, v22, v23
	v_cvt_pk_f16_f32 v22, v20, v21
	s_waitcnt vmcnt(14)
	v_cvt_pk_f16_f32 v21, v26, v27
	v_cvt_pk_f16_f32 v20, v24, v25
	s_lshl_b32 s0, s0, 2
	s_waitcnt lgkmcnt(0)
	s_barrier
	ds_write2st64_b64 v0, v[22:23], v[20:21] offset0:80 offset1:84
	s_waitcnt vmcnt(13)
	v_cvt_pk_f16_f32 v20, v28, v29
	v_lshl_add_u64 v[28:29], v[2:3], 0, s[0:1]
	v_cvt_pk_f16_f32 v21, v30, v31
	v_add_co_u32_e32 v30, vcc, s3, v28
	s_waitcnt vmcnt(12)
	v_cvt_pk_f16_f32 v23, v34, v35
	v_cvt_pk_f16_f32 v22, v32, v33
	v_addc_co_u32_e32 v31, vcc, 0, v29, vcc
	ds_write2st64_b64 v0, v[20:21], v[22:23] offset0:88 offset1:92
	v_add_co_u32_e32 v68, vcc, s4, v28
	global_load_dwordx4 v[20:23], v[28:29], off sc1 nt
	global_load_dwordx4 v[24:27], v[30:31], off sc1 nt
	v_addc_co_u32_e32 v69, vcc, 0, v29, vcc
	s_add_i32 s0, s2, 0x280
	v_add_co_u32_e32 v70, vcc, s5, v28
	s_and_b32 s0, s0, 0x3c0
	s_nop 0
	v_addc_co_u32_e32 v71, vcc, 0, v29, vcc
	global_load_dwordx4 v[28:31], v[68:69], off sc1 nt
	global_load_dwordx4 v[32:35], v[70:71], off sc1 nt
	s_waitcnt vmcnt(15)
	v_cvt_pk_f16_f32 v39, v38, v39
	v_cvt_pk_f16_f32 v38, v36, v37
	s_waitcnt vmcnt(14)
	v_cvt_pk_f16_f32 v37, v42, v43
	v_cvt_pk_f16_f32 v36, v40, v41
	s_lshl_b32 s0, s0, 2
	s_waitcnt lgkmcnt(0)
	s_barrier
	ds_write2st64_b64 v0, v[38:39], v[36:37] offset0:96 offset1:100
	s_waitcnt vmcnt(13)
	v_cvt_pk_f16_f32 v36, v44, v45
	v_lshl_add_u64 v[44:45], v[2:3], 0, s[0:1]
	v_cvt_pk_f16_f32 v37, v46, v47
	v_add_co_u32_e32 v46, vcc, s3, v44
	s_waitcnt vmcnt(12)
	v_cvt_pk_f16_f32 v39, v50, v51
	v_cvt_pk_f16_f32 v38, v48, v49
	v_addc_co_u32_e32 v47, vcc, 0, v45, vcc
	ds_write2st64_b64 v0, v[36:37], v[38:39] offset0:104 offset1:108
	v_add_co_u32_e32 v68, vcc, s4, v44
	global_load_dwordx4 v[36:39], v[44:45], off sc1 nt
	global_load_dwordx4 v[40:43], v[46:47], off sc1 nt
	v_addc_co_u32_e32 v69, vcc, 0, v45, vcc
	v_add_co_u32_e32 v70, vcc, s5, v44
	s_add_i32 s0, s2, 0x2c0
	s_nop 0
	v_addc_co_u32_e32 v71, vcc, 0, v45, vcc
	global_load_dwordx4 v[44:47], v[68:69], off sc1 nt
	global_load_dwordx4 v[48:51], v[70:71], off sc1 nt
	s_and_b32 s0, s0, 0x3c0
	s_waitcnt vmcnt(15)
	v_cvt_pk_f16_f32 v55, v54, v55
	v_cvt_pk_f16_f32 v54, v52, v53
	s_waitcnt vmcnt(14)
	v_cvt_pk_f16_f32 v53, v58, v59
	v_cvt_pk_f16_f32 v52, v56, v57
	s_lshl_b32 s0, s0, 2
	s_waitcnt lgkmcnt(0)
	s_barrier
	ds_write2st64_b64 v0, v[54:55], v[52:53] offset0:112 offset1:116
	s_waitcnt vmcnt(13)
	v_cvt_pk_f16_f32 v53, v62, v63
	v_cvt_pk_f16_f32 v52, v60, v61
	s_waitcnt vmcnt(12)
	v_cvt_pk_f16_f32 v55, v66, v67
	v_cvt_pk_f16_f32 v54, v64, v65
	v_lshl_add_u64 v[60:61], v[2:3], 0, s[0:1]
	ds_write2st64_b64 v0, v[52:53], v[54:55] offset0:120 offset1:124
	v_add_co_u32_e32 v62, vcc, s3, v60
	s_add_i32 s0, s2, 0x300
	s_nop 0
	v_addc_co_u32_e32 v63, vcc, 0, v61, vcc
	global_load_dwordx4 v[52:55], v[60:61], off sc1 nt
	global_load_dwordx4 v[56:59], v[62:63], off sc1 nt
	v_add_co_u32_e32 v68, vcc, s4, v60
	s_waitcnt vmcnt(13)
	v_cvt_pk_f16_f32 v7, v6, v7
	v_addc_co_u32_e32 v69, vcc, 0, v61, vcc
	v_add_co_u32_e32 v70, vcc, s5, v60
	v_cvt_pk_f16_f32 v6, v4, v5
	s_and_b32 s0, s0, 0x3c0
	v_addc_co_u32_e32 v71, vcc, 0, v61, vcc
	global_load_dwordx4 v[60:63], v[68:69], off sc1 nt
	global_load_dwordx4 v[64:67], v[70:71], off sc1 nt
	s_waitcnt lgkmcnt(0)
	s_barrier
	ds_write_b64 v1, v[6:7]
	s_waitcnt vmcnt(14)
	v_cvt_pk_f16_f32 v5, v10, v11
	v_cvt_pk_f16_f32 v4, v8, v9
	v_add_u32_e32 v1, 0x10800, v0
	s_lshl_b32 s0, s0, 2
	ds_write_b64 v1, v[4:5]
	s_waitcnt vmcnt(13)
	v_cvt_pk_f16_f32 v4, v12, v13
	v_lshl_add_u64 v[12:13], v[2:3], 0, s[0:1]
	v_cvt_pk_f16_f32 v5, v14, v15
	v_add_co_u32_e32 v14, vcc, s3, v12
	v_add_u32_e32 v1, 0x11000, v0
	s_nop 0
	v_addc_co_u32_e32 v15, vcc, 0, v13, vcc
	v_add_co_u32_e32 v68, vcc, s4, v12
	ds_write_b64 v1, v[4:5]
	s_waitcnt vmcnt(12)
	v_cvt_pk_f16_f32 v5, v18, v19
	v_cvt_pk_f16_f32 v4, v16, v17
	v_add_u32_e32 v1, 0x11800, v0
	v_addc_co_u32_e32 v69, vcc, 0, v13, vcc
	s_add_i32 s0, s2, 0x340
	ds_write_b64 v1, v[4:5]
	v_add_co_u32_e32 v70, vcc, s5, v12
	s_waitcnt vmcnt(11)
	v_cvt_pk_f16_f32 v23, v22, v23
	v_cvt_pk_f16_f32 v22, v20, v21
	v_add_u32_e32 v1, 0x12000, v0
	s_and_b32 s0, s0, 0x3c0
	global_load_dwordx4 v[4:7], v[12:13], off sc1 nt
	global_load_dwordx4 v[8:11], v[14:15], off sc1 nt
	v_addc_co_u32_e32 v71, vcc, 0, v13, vcc
	global_load_dwordx4 v[12:15], v[68:69], off sc1 nt
	global_load_dwordx4 v[16:19], v[70:71], off sc1 nt
	s_waitcnt lgkmcnt(0)
	s_barrier
	ds_write_b64 v1, v[22:23]
	s_waitcnt vmcnt(14)
	v_cvt_pk_f16_f32 v21, v26, v27
	v_cvt_pk_f16_f32 v20, v24, v25
	v_add_u32_e32 v1, 0x12800, v0
	s_lshl_b32 s0, s0, 2
	ds_write_b64 v1, v[20:21]
	s_waitcnt vmcnt(13)
	v_cvt_pk_f16_f32 v20, v28, v29
	v_lshl_add_u64 v[28:29], v[2:3], 0, s[0:1]
	v_cvt_pk_f16_f32 v21, v30, v31
	v_add_co_u32_e32 v30, vcc, s3, v28
	v_add_u32_e32 v1, 0x13000, v0
	s_nop 0
	v_addc_co_u32_e32 v31, vcc, 0, v29, vcc
	v_add_co_u32_e32 v68, vcc, s4, v28
	ds_write_b64 v1, v[20:21]
	s_waitcnt vmcnt(12)
	v_cvt_pk_f16_f32 v21, v34, v35
	v_cvt_pk_f16_f32 v20, v32, v33
	v_add_u32_e32 v1, 0x13800, v0
	v_addc_co_u32_e32 v69, vcc, 0, v29, vcc
	s_add_i32 s0, s2, 0x380
	ds_write_b64 v1, v[20:21]
	v_add_co_u32_e32 v70, vcc, s5, v28
	s_waitcnt vmcnt(11)
	v_cvt_pk_f16_f32 v39, v38, v39
	v_cvt_pk_f16_f32 v38, v36, v37
	v_add_u32_e32 v1, 0x14000, v0
	s_and_b32 s0, s0, 0x3c0
	global_load_dwordx4 v[20:23], v[28:29], off sc1 nt
	global_load_dwordx4 v[24:27], v[30:31], off sc1 nt
	v_addc_co_u32_e32 v71, vcc, 0, v29, vcc
	global_load_dwordx4 v[28:31], v[68:69], off sc1 nt
	global_load_dwordx4 v[32:35], v[70:71], off sc1 nt
	s_waitcnt lgkmcnt(0)
	s_barrier
	ds_write_b64 v1, v[38:39]
	s_waitcnt vmcnt(14)
	v_cvt_pk_f16_f32 v37, v42, v43
	v_cvt_pk_f16_f32 v36, v40, v41
	v_add_u32_e32 v1, 0x14800, v0
	s_lshl_b32 s0, s0, 2
	ds_write_b64 v1, v[36:37]
	s_waitcnt vmcnt(13)
	v_cvt_pk_f16_f32 v36, v44, v45
	v_lshl_add_u64 v[44:45], v[2:3], 0, s[0:1]
	v_cvt_pk_f16_f32 v37, v46, v47
	v_add_co_u32_e32 v46, vcc, s3, v44
	s_addk_i32 s2, 0x3c0
	s_nop 0
	v_addc_co_u32_e32 v47, vcc, 0, v45, vcc
	v_add_co_u32_e32 v68, vcc, s4, v44
	v_add_u32_e32 v1, 0x15000, v0
	s_nop 0
	v_addc_co_u32_e32 v69, vcc, 0, v45, vcc
	s_and_b32 s0, s2, 0x3c0
	ds_write_b64 v1, v[36:37]
	s_waitcnt vmcnt(12)
	v_cvt_pk_f16_f32 v37, v50, v51
	v_cvt_pk_f16_f32 v36, v48, v49
	v_add_u32_e32 v1, 0x15800, v0
	v_add_co_u32_e32 v70, vcc, s5, v44
	s_lshl_b32 s0, s0, 2
	ds_write_b64 v1, v[36:37]
	v_addc_co_u32_e32 v71, vcc, 0, v45, vcc
	v_lshl_add_u64 v[2:3], v[2:3], 0, s[0:1]
	global_load_dwordx4 v[36:39], v[44:45], off sc1 nt
	global_load_dwordx4 v[40:43], v[46:47], off sc1 nt
	s_waitcnt vmcnt(13)
	v_cvt_pk_f16_f32 v55, v54, v55
	v_cvt_pk_f16_f32 v54, v52, v53
	s_waitcnt vmcnt(12)
	v_cvt_pk_f16_f32 v52, v56, v57
	v_add_co_u32_e32 v56, vcc, s3, v2
	v_add_u32_e32 v1, 0x16000, v0
	s_nop 0
	v_addc_co_u32_e32 v57, vcc, 0, v3, vcc
	global_load_dwordx4 v[44:47], v[68:69], off sc1 nt
	global_load_dwordx4 v[48:51], v[70:71], off sc1 nt
	s_waitcnt lgkmcnt(0)
	s_barrier
	ds_write_b64 v1, v[54:55]
	v_cvt_pk_f16_f32 v53, v58, v59
	v_add_u32_e32 v1, 0x16800, v0
	v_add_co_u32_e32 v68, vcc, s4, v2
	ds_write_b64 v1, v[52:53]
	global_load_dwordx4 v[52:55], v[2:3], off sc1 nt
	v_addc_co_u32_e32 v69, vcc, 0, v3, vcc
	global_load_dwordx4 v[56:59], v[56:57], off sc1 nt
	v_add_co_u32_e32 v2, vcc, s5, v2
	global_load_dwordx4 v[68:71], v[68:69], off sc1 nt
	s_nop 0
	v_addc_co_u32_e32 v3, vcc, 0, v3, vcc
	global_load_dwordx4 v[72:75], v[2:3], off sc1 nt
	s_waitcnt vmcnt(17)
	v_cvt_pk_f16_f32 v63, v62, v63
	v_cvt_pk_f16_f32 v62, v60, v61
	v_add_u32_e32 v1, 0x17000, v0
	ds_write_b64 v1, v[62:63]
	s_waitcnt vmcnt(16)
	v_cvt_pk_f16_f32 v3, v66, v67
	v_cvt_pk_f16_f32 v2, v64, v65
	v_add_u32_e32 v1, 0x17800, v0
	ds_write_b64 v1, v[2:3]
	s_waitcnt vmcnt(15)
	v_cvt_pk_f16_f32 v3, v6, v7
	v_cvt_pk_f16_f32 v2, v4, v5
	v_add_u32_e32 v1, 0x18000, v0
	s_waitcnt lgkmcnt(0)
	s_barrier
	ds_write_b64 v1, v[2:3]
	s_waitcnt vmcnt(14)
	v_cvt_pk_f16_f32 v3, v10, v11
	v_cvt_pk_f16_f32 v2, v8, v9
	v_add_u32_e32 v1, 0x18800, v0
	ds_write_b64 v1, v[2:3]
	s_waitcnt vmcnt(13)
	v_cvt_pk_f16_f32 v3, v14, v15
	v_cvt_pk_f16_f32 v2, v12, v13
	v_add_u32_e32 v1, 0x19000, v0
	ds_write_b64 v1, v[2:3]
	s_waitcnt vmcnt(12)
	v_cvt_pk_f16_f32 v3, v18, v19
	v_cvt_pk_f16_f32 v2, v16, v17
	v_add_u32_e32 v1, 0x19800, v0
	ds_write_b64 v1, v[2:3]
	s_waitcnt vmcnt(11)
	v_cvt_pk_f16_f32 v3, v22, v23
	v_cvt_pk_f16_f32 v2, v20, v21
	v_add_u32_e32 v1, 0x1a000, v0
	s_waitcnt lgkmcnt(0)
	s_barrier
	ds_write_b64 v1, v[2:3]
	s_waitcnt vmcnt(10)
	v_cvt_pk_f16_f32 v3, v26, v27
	v_cvt_pk_f16_f32 v2, v24, v25
	v_add_u32_e32 v1, 0x1a800, v0
	ds_write_b64 v1, v[2:3]
	s_waitcnt vmcnt(9)
	v_cvt_pk_f16_f32 v3, v30, v31
	v_cvt_pk_f16_f32 v2, v28, v29
	v_add_u32_e32 v1, 0x1b000, v0
	ds_write_b64 v1, v[2:3]
	s_waitcnt vmcnt(8)
	v_cvt_pk_f16_f32 v3, v34, v35
	v_cvt_pk_f16_f32 v2, v32, v33
	v_add_u32_e32 v1, 0x1b800, v0
	ds_write_b64 v1, v[2:3]
	v_add_u32_e32 v1, 0x1c000, v0
	s_waitcnt lgkmcnt(0)
	s_barrier
	s_waitcnt vmcnt(7)
	v_cvt_pk_f16_f32 v3, v38, v39
	v_cvt_pk_f16_f32 v2, v36, v37
	ds_write_b64 v1, v[2:3]
	s_waitcnt vmcnt(6)
	v_cvt_pk_f16_f32 v3, v42, v43
	v_cvt_pk_f16_f32 v2, v40, v41
	v_add_u32_e32 v1, 0x1c800, v0
	ds_write_b64 v1, v[2:3]
	v_add_u32_e32 v1, 0x1d000, v0
	s_waitcnt vmcnt(5)
	v_cvt_pk_f16_f32 v3, v46, v47
	v_cvt_pk_f16_f32 v2, v44, v45
	ds_write_b64 v1, v[2:3]
	s_waitcnt vmcnt(4)
	v_cvt_pk_f16_f32 v3, v50, v51
	v_cvt_pk_f16_f32 v2, v48, v49
	v_add_u32_e32 v1, 0x1d800, v0
	ds_write_b64 v1, v[2:3]
	v_add_u32_e32 v1, 0x1e000, v0
	s_waitcnt lgkmcnt(0)
	s_barrier
	s_waitcnt vmcnt(3)
	v_cvt_pk_f16_f32 v3, v54, v55
	v_cvt_pk_f16_f32 v2, v52, v53
	ds_write_b64 v1, v[2:3]
	s_waitcnt vmcnt(2)
	v_cvt_pk_f16_f32 v3, v58, v59
	v_cvt_pk_f16_f32 v2, v56, v57
	v_add_u32_e32 v1, 0x1e800, v0
	ds_write_b64 v1, v[2:3]
	s_waitcnt vmcnt(1)
	v_cvt_pk_f16_f32 v3, v70, v71
	v_cvt_pk_f16_f32 v2, v68, v69
	v_add_u32_e32 v1, 0x1f000, v0
	ds_write_b64 v1, v[2:3]
	s_waitcnt vmcnt(0)
	v_cvt_pk_f16_f32 v3, v74, v75
	v_cvt_pk_f16_f32 v2, v72, v73
	v_add_u32_e32 v0, 0x1f800, v0
	ds_write_b64 v0, v[2:3]
	s_waitcnt lgkmcnt(0)
	s_barrier
	s_endpgm
